# MoBA past-block sub-tiles rewritten: unselected rows start at -inf (1 select instead of 16), scores and weights kept in place
# speedup vs baseline: 1.0123x; 1.0083x over previous
; __device__ __forceinline__ float max2_raw(float a, float b) { float d; asm("v_max_f32 %0, %1, %2" : "=v"(d) : "v"(a), "v"(b)); return d; }
; template <int MODE>
; __device__ __forceinline__ void attn_moba_sub(const bf16x8 (&qr)[4], f32x16& O0, f32x16& O1, float& m, float& l, unsigned saddr, int j, int kv0, int q, int q0, int hi, float slope2, bool rowok) {
;     ...
;     f32x16 S; const float sbase = slope2 * (float)(kv0 + 8 * hi - q0);
; #pragma unroll
;     for (int r = 0; r < 16; ++r) S[r] = sbase + slope2 * (float)((r & 7) + 16 * (r >> 3));
; #pragma unroll
;     for (int d0 = 0; d0 < 4; ++d0) S = __builtin_amdgcn_mfma_f32_32x32x16_bf16(kf[d0], qr[d0], S, 0, 0, 0);
;     if (MODE == 1) {
; #pragma unroll
;         for (int r = 0; r < 16; ++r) { const int key = kv0 + (r & 7) + 8 * hi + 16 * (r >> 3); if (key > q) S[r] = -INFINITY; }
;     }
;     if (MODE == 2) { if (!rowok) {
; #pragma unroll
;         for (int r = 0; r < 16; ++r) S[r] = -INFINITY; } }
;     float rm = rowmax16_raw(S);
;     { const auto rr = __builtin_amdgcn_permlane32_swap(__float_as_uint(rm), __float_as_uint(rm), false, false); rm = max2_raw(__uint_as_float(rr[0]), __uint_as_float(rr[1])); }
;     if (__any(rm > m)) { const float mn = fmaxf(fmaxf(m, rm), -1e30f); const float alpha = __builtin_amdgcn_exp2f(m - mn); l *= alpha; O0 *= alpha; O1 *= alpha; m = mn; }
; __device__ __forceinline__ void attn_moba_unit(Frame& F, const bf16_t* Qh, const bf16_t* Kh, const bf16_t* Vth, const float* KMh, const float slope2, const int qb, bf16_t* AOp) {
;     ...
;         } else if ((wsel >> (T >> 2)) & 1u) {
;             const bool rowok = (sel >> (T >> 2)) & 1u;
;             attn_moba_sub<2>(qr, O0, O1, m, l, sa, 1, 64 * T + 32, q, q0, hi, slope2, rowok); attn_moba_sub<2>(qr, O0, O1, m, l, sa, 0, 64 * T, q, q0, hi, slope2, rowok);
.LBB0_1331:
	s_lshr_b32 s0, s92, 2
	s_lshl_b32 s0, 1, s0
	s_and_b32 s1, s0, s79
	s_cmp_eq_u32 s1, 0
	s_cbranch_scc1 .LBB0_1337
	v_add_u32_e32 v113, s89, v195
	s_nop 1
	v_add_u32_e32 v80, 0xe0, v113
	v_cvt_f32_i32_e32 v80, v80
	v_add_u32_e32 v81, 0x1000, v198
	v_add_u32_e32 v82, 0x3000, v198
	ds_read_b128 v[114:117], v81
	ds_read_b128 v[118:121], v81 offset:1024
	ds_read_b128 v[122:125], v81 offset:2048
	ds_read_b128 v[144:147], v81 offset:3072
	ds_read_b128 v[108:111], v82
	ds_read_b128 v[100:103], v82 offset:1024
	ds_read_b128 v[104:107], v82 offset:2048
	ds_read_b128 v[96:99], v82 offset:3072
	s_waitcnt lgkmcnt(4)
	v_and_b32_e32 v112, s0, v193
	v_cmp_eq_u32_e64 s[70:71], 0, v112
	v_mul_f32_e32 v80, v163, v80
	s_nop 0
	v_cndmask_b32_e64 v80, v80, v190, s[70:71]
	v_pk_add_f32 v[94:95], v[176:177], v[80:81] op_sel_hi:[1,0]
	v_pk_add_f32 v[92:93], v[174:175], v[80:81] op_sel_hi:[1,0]
	v_pk_add_f32 v[90:91], v[172:173], v[80:81] op_sel_hi:[1,0]
	v_pk_add_f32 v[88:89], v[170:171], v[80:81] op_sel_hi:[1,0]
	v_pk_add_f32 v[86:87], v[168:169], v[80:81] op_sel_hi:[1,0]
	v_pk_add_f32 v[84:85], v[166:167], v[80:81] op_sel_hi:[1,0]
	v_pk_add_f32 v[82:83], v[164:165], v[80:81] op_sel_hi:[1,0]
	v_pk_add_f32 v[80:81], v[162:163], v[80:81] op_sel_hi:[1,0]
	s_nop 1
	v_mfma_f32_32x32x16_bf16 v[80:95], v[114:117], v[128:131], v[80:95]
	v_mfma_f32_32x32x16_bf16 v[80:95], v[118:121], v[132:135], v[80:95]
	v_mfma_f32_32x32x16_bf16 v[80:95], v[122:125], v[136:139], v[80:95]
	v_mfma_f32_32x32x16_bf16 v[80:95], v[144:147], v[140:143], v[80:95]
	s_nop 11
	v_max3_f32 v114, v80, v81, v82
	v_max3_f32 v115, v83, v84, v85
	v_max3_f32 v116, v86, v87, v88
	v_max3_f32 v114, v114, v115, v116
	v_max3_f32 v115, v89, v90, v91
	v_max3_f32 v116, v92, v93, v94
	v_max3_f32 v115, v115, v116, v95
	v_max_f32_e32 v114, v114, v115
	v_mov_b32_e32 v115, v114
	s_nop 1
	v_permlane32_swap_b32_e32 v114, v115
	v_max_f32_e32 v115, v114, v115
	v_cmp_gt_f32_e32 vcc, v115, v196
	s_cbranch_vccz .Lmoba_m2_1
	v_max3_f32 v119, v196, v115, s86
	v_sub_f32_e32 v118, v196, v119
	v_exp_f32_e32 v118, v118
	v_mov_b32_e32 v196, v119
	v_mul_f32_e32 v197, v197, v118
	v_pk_mul_f32 v[62:63], v[62:63], v[118:119] op_sel_hi:[1,0]
	v_pk_mul_f32 v[60:61], v[60:61], v[118:119] op_sel_hi:[1,0]
	v_pk_mul_f32 v[58:59], v[58:59], v[118:119] op_sel_hi:[1,0]
	v_pk_mul_f32 v[56:57], v[56:57], v[118:119] op_sel_hi:[1,0]
	v_pk_mul_f32 v[54:55], v[54:55], v[118:119] op_sel_hi:[1,0]
	v_pk_mul_f32 v[52:53], v[52:53], v[118:119] op_sel_hi:[1,0]
	v_pk_mul_f32 v[50:51], v[50:51], v[118:119] op_sel_hi:[1,0]
	v_pk_mul_f32 v[48:49], v[48:49], v[118:119] op_sel_hi:[1,0]
	v_pk_mul_f32 v[78:79], v[78:79], v[118:119] op_sel_hi:[1,0]
	v_pk_mul_f32 v[76:77], v[76:77], v[118:119] op_sel_hi:[1,0]
	v_pk_mul_f32 v[74:75], v[74:75], v[118:119] op_sel_hi:[1,0]
	v_pk_mul_f32 v[72:73], v[72:73], v[118:119] op_sel_hi:[1,0]
	v_pk_mul_f32 v[70:71], v[70:71], v[118:119] op_sel_hi:[1,0]
	v_pk_mul_f32 v[68:69], v[68:69], v[118:119] op_sel_hi:[1,0]
	v_pk_mul_f32 v[66:67], v[66:67], v[118:119] op_sel_hi:[1,0]
	v_pk_mul_f32 v[64:65], v[64:65], v[118:119] op_sel_hi:[1,0]
; __device__ __forceinline__ unsigned pk2(float lo, float hi) { const f32x2_pk v = {lo, hi}; return __builtin_bit_cast(unsigned, __builtin_convertvector(v, bf16x2)); }
; template <int MODE>
; __device__ __forceinline__ void attn_moba_sub(const bf16x8 (&qr)[4], f32x16& O0, f32x16& O1, float& m, float& l, unsigned saddr, int j, int kv0, int q, int q0, int hi, float slope2, bool rowok) {
;     ...
;     if (__any(rm > m)) { const float mn = fmaxf(fmaxf(m, rm), -1e30f); const float alpha = __builtin_amdgcn_exp2f(m - mn); l *= alpha; O0 *= alpha; O1 *= alpha; m = mn; }
;     float p[16]; float ps = 0.f;
; #pragma unroll
;     for (int r = 0; r < 16; ++r) { p[r] = __builtin_amdgcn_exp2f(S[r] - m); ps += p[r]; }
;     l += ps;
;     u32x4 w0, w1;
;     w0.x = pk2(p[0], p[1]); w0.y = pk2(p[2], p[3]); w0.z = pk2(p[4], p[5]); w0.w = pk2(p[6], p[7]);
;     w1.x = pk2(p[8], p[9]); w1.y = pk2(p[10], p[11]); w1.z = pk2(p[12], p[13]); w1.w = pk2(p[14], p[15]);
;     const bf16x8 pf0 = __builtin_bit_cast(bf16x8, w0), pf1 = __builtin_bit_cast(bf16x8, w1);
;     O0 = __builtin_amdgcn_mfma_f32_32x32x16_bf16(vf[0][0], pf0, O0, 0, 0, 0); O0 = __builtin_amdgcn_mfma_f32_32x32x16_bf16(vf[1][0], pf1, O0, 0, 0, 0);
;     O1 = __builtin_amdgcn_mfma_f32_32x32x16_bf16(vf[0][1], pf0, O1, 0, 0, 0); O1 = __builtin_amdgcn_mfma_f32_32x32x16_bf16(vf[1][1], pf1, O1, 0, 0, 0);
.Lmoba_m2_1:
	v_sub_f32_e32 v80, v80, v196
	v_exp_f32_e32 v80, v80
	v_sub_f32_e32 v81, v81, v196
	v_exp_f32_e32 v81, v81
	v_sub_f32_e32 v82, v82, v196
	v_exp_f32_e32 v82, v82
	v_sub_f32_e32 v83, v83, v196
	v_exp_f32_e32 v83, v83
	v_add_f32_e32 v117, 0, v80
	v_sub_f32_e32 v84, v84, v196
	v_exp_f32_e32 v84, v84
	v_add_f32_e32 v117, v81, v117
	v_sub_f32_e32 v85, v85, v196
	v_exp_f32_e32 v85, v85
	v_add_f32_e32 v117, v82, v117
	v_sub_f32_e32 v86, v86, v196
	v_exp_f32_e32 v86, v86
	v_add_f32_e32 v117, v83, v117
	v_sub_f32_e32 v87, v87, v196
	v_exp_f32_e32 v87, v87
	v_add_f32_e32 v117, v84, v117
	v_sub_f32_e32 v88, v88, v196
	v_exp_f32_e32 v88, v88
	v_add_f32_e32 v117, v85, v117
	v_sub_f32_e32 v89, v89, v196
	v_exp_f32_e32 v89, v89
	v_add_f32_e32 v117, v86, v117
	v_sub_f32_e32 v90, v90, v196
	v_exp_f32_e32 v90, v90
	v_add_f32_e32 v117, v87, v117
	v_sub_f32_e32 v91, v91, v196
	v_exp_f32_e32 v91, v91
	v_cvt_pk_bf16_f32 v80, v80, v81
	v_cvt_pk_bf16_f32 v81, v82, v83
	v_cvt_pk_bf16_f32 v82, v84, v85
	v_cvt_pk_bf16_f32 v83, v86, v87
	v_add_f32_e32 v117, v88, v117
	v_sub_f32_e32 v92, v92, v196
	v_exp_f32_e32 v92, v92
	s_waitcnt lgkmcnt(0)
	v_mfma_f32_32x32x16_bf16 v[48:63], v[108:111], v[80:83], v[48:63]
	v_add_f32_e32 v117, v89, v117
	v_sub_f32_e32 v93, v93, v196
	v_exp_f32_e32 v93, v93
	v_add_f32_e32 v117, v90, v117
	v_sub_f32_e32 v94, v94, v196
	v_exp_f32_e32 v94, v94
	v_add_f32_e32 v117, v91, v117
	v_sub_f32_e32 v95, v95, v196
	v_exp_f32_e32 v95, v95
	v_mfma_f32_32x32x16_bf16 v[64:79], v[100:103], v[80:83], v[64:79]
	v_add_u32_e32 v80, 0x2000, v198
	v_add_f32_e32 v117, v92, v117
	v_add_f32_e32 v117, v93, v117
	v_add_f32_e32 v117, v94, v117
	v_add_f32_e32 v117, v95, v117
	v_cvt_pk_bf16_f32 v84, v88, v89
	v_cvt_pk_bf16_f32 v85, v90, v91
	v_cvt_pk_bf16_f32 v86, v92, v93
	v_cvt_pk_bf16_f32 v87, v94, v95
	v_add_f32_e32 v112, v197, v117
	s_nop 0
	v_mfma_f32_32x32x16_bf16 v[48:63], v[104:107], v[84:87], v[48:63]
	v_mfma_f32_32x32x16_bf16 v[64:79], v[96:99], v[84:87], v[64:79]
	ds_read_b128 v[114:117], v198
	ds_read_b128 v[118:121], v198 offset:1024
	ds_read_b128 v[122:125], v198 offset:2048
	ds_read_b128 v[144:147], v198 offset:3072
	ds_read_b128 v[108:111], v80
	ds_read_b128 v[100:103], v80 offset:1024
	ds_read_b128 v[104:107], v80 offset:2048
	ds_read_b128 v[96:99], v80 offset:3072
	s_waitcnt lgkmcnt(4)
	v_add_u32_e32 v80, 0xc0, v113
	v_cvt_f32_i32_e32 v80, v80
	v_mul_f32_e32 v80, v163, v80
	v_cndmask_b32_e64 v80, v80, v190, s[70:71]
	v_pk_add_f32 v[94:95], v[176:177], v[80:81] op_sel_hi:[1,0]
	v_pk_add_f32 v[92:93], v[174:175], v[80:81] op_sel_hi:[1,0]
	v_pk_add_f32 v[90:91], v[172:173], v[80:81] op_sel_hi:[1,0]
	v_pk_add_f32 v[88:89], v[170:171], v[80:81] op_sel_hi:[1,0]
	v_pk_add_f32 v[86:87], v[168:169], v[80:81] op_sel_hi:[1,0]
	v_pk_add_f32 v[84:85], v[166:167], v[80:81] op_sel_hi:[1,0]
	v_pk_add_f32 v[82:83], v[164:165], v[80:81] op_sel_hi:[1,0]
	v_pk_add_f32 v[80:81], v[162:163], v[80:81] op_sel_hi:[1,0]
	s_nop 1
	v_mfma_f32_32x32x16_bf16 v[80:95], v[114:117], v[128:131], v[80:95]
	v_mfma_f32_32x32x16_bf16 v[80:95], v[118:121], v[132:135], v[80:95]
	v_mfma_f32_32x32x16_bf16 v[80:95], v[122:125], v[136:139], v[80:95]
	v_mfma_f32_32x32x16_bf16 v[80:95], v[144:147], v[140:143], v[80:95]
	s_nop 11
	v_max3_f32 v114, v80, v81, v82
	v_max3_f32 v115, v83, v84, v85
	v_max3_f32 v116, v86, v87, v88
	v_max3_f32 v114, v114, v115, v116
	v_max3_f32 v115, v89, v90, v91
	v_max3_f32 v116, v92, v93, v94
	v_max3_f32 v115, v115, v116, v95
	v_max_f32_e32 v114, v114, v115
	v_mov_b32_e32 v115, v114
	s_nop 1
	v_permlane32_swap_b32_e32 v114, v115
	v_max_f32_e32 v115, v114, v115
	v_cmp_gt_f32_e32 vcc, v115, v196
	s_cbranch_vccz .Lmoba_m2_2
	v_max3_f32 v119, v196, v115, s86
	v_sub_f32_e32 v118, v196, v119
	v_exp_f32_e32 v118, v118
	v_mov_b32_e32 v196, v119
	v_mul_f32_e32 v112, v118, v112
	v_pk_mul_f32 v[62:63], v[62:63], v[118:119] op_sel_hi:[1,0]
	v_pk_mul_f32 v[60:61], v[60:61], v[118:119] op_sel_hi:[1,0]
	v_pk_mul_f32 v[58:59], v[58:59], v[118:119] op_sel_hi:[1,0]
	v_pk_mul_f32 v[56:57], v[56:57], v[118:119] op_sel_hi:[1,0]
	v_pk_mul_f32 v[54:55], v[54:55], v[118:119] op_sel_hi:[1,0]
	v_pk_mul_f32 v[52:53], v[52:53], v[118:119] op_sel_hi:[1,0]
	v_pk_mul_f32 v[50:51], v[50:51], v[118:119] op_sel_hi:[1,0]
	v_pk_mul_f32 v[48:49], v[48:49], v[118:119] op_sel_hi:[1,0]
	v_pk_mul_f32 v[78:79], v[78:79], v[118:119] op_sel_hi:[1,0]
	v_pk_mul_f32 v[76:77], v[76:77], v[118:119] op_sel_hi:[1,0]
	v_pk_mul_f32 v[74:75], v[74:75], v[118:119] op_sel_hi:[1,0]
	v_pk_mul_f32 v[72:73], v[72:73], v[118:119] op_sel_hi:[1,0]
	v_pk_mul_f32 v[70:71], v[70:71], v[118:119] op_sel_hi:[1,0]
	v_pk_mul_f32 v[68:69], v[68:69], v[118:119] op_sel_hi:[1,0]
	v_pk_mul_f32 v[66:67], v[66:67], v[118:119] op_sel_hi:[1,0]
	v_pk_mul_f32 v[64:65], v[64:65], v[118:119] op_sel_hi:[1,0]
.Lmoba_m2_2:
	v_sub_f32_e32 v80, v80, v196
	v_exp_f32_e32 v80, v80
	v_sub_f32_e32 v81, v81, v196
	v_exp_f32_e32 v81, v81
	v_sub_f32_e32 v82, v82, v196
	v_exp_f32_e32 v82, v82
	v_sub_f32_e32 v83, v83, v196
	v_exp_f32_e32 v83, v83
	v_add_f32_e32 v117, 0, v80
	v_sub_f32_e32 v84, v84, v196
	v_exp_f32_e32 v84, v84
	v_add_f32_e32 v117, v81, v117
	v_sub_f32_e32 v85, v85, v196
	v_exp_f32_e32 v85, v85
	v_add_f32_e32 v117, v82, v117
	v_sub_f32_e32 v86, v86, v196
	v_exp_f32_e32 v86, v86
	v_add_f32_e32 v117, v83, v117
	v_sub_f32_e32 v87, v87, v196
	v_exp_f32_e32 v87, v87
	v_add_f32_e32 v117, v84, v117
	v_sub_f32_e32 v88, v88, v196
	v_exp_f32_e32 v88, v88
	v_add_f32_e32 v117, v85, v117
	v_sub_f32_e32 v89, v89, v196
	v_exp_f32_e32 v89, v89
	v_add_f32_e32 v117, v86, v117
	v_sub_f32_e32 v90, v90, v196
	v_exp_f32_e32 v90, v90
	v_add_f32_e32 v117, v87, v117
	v_sub_f32_e32 v91, v91, v196
	v_exp_f32_e32 v91, v91
	v_cvt_pk_bf16_f32 v80, v80, v81
	v_cvt_pk_bf16_f32 v81, v82, v83
	v_cvt_pk_bf16_f32 v82, v84, v85
	v_cvt_pk_bf16_f32 v83, v86, v87
	v_add_f32_e32 v117, v88, v117
	v_sub_f32_e32 v92, v92, v196
	v_exp_f32_e32 v92, v92
	s_waitcnt lgkmcnt(0)
	v_mfma_f32_32x32x16_bf16 v[48:63], v[108:111], v[80:83], v[48:63]
	v_add_f32_e32 v117, v89, v117
	v_sub_f32_e32 v93, v93, v196
	v_exp_f32_e32 v93, v93
	v_add_f32_e32 v117, v90, v117
	v_sub_f32_e32 v94, v94, v196
	v_exp_f32_e32 v94, v94
	v_add_f32_e32 v117, v91, v117
	v_sub_f32_e32 v95, v95, v196
	v_exp_f32_e32 v95, v95
	v_mfma_f32_32x32x16_bf16 v[64:79], v[100:103], v[80:83], v[64:79]
	v_add_f32_e32 v117, v92, v117
	v_add_f32_e32 v117, v93, v117
	v_add_f32_e32 v117, v94, v117
	v_add_f32_e32 v117, v95, v117
	v_cvt_pk_bf16_f32 v84, v88, v89
	v_cvt_pk_bf16_f32 v85, v90, v91
	v_cvt_pk_bf16_f32 v86, v92, v93
	v_cvt_pk_bf16_f32 v87, v94, v95
	v_add_f32_e32 v197, v112, v117
	s_nop 0
	v_mfma_f32_32x32x16_bf16 v[48:63], v[104:107], v[84:87], v[48:63]
	v_mfma_f32_32x32x16_bf16 v[64:79], v[96:99], v[84:87], v[64:79]
